# edge1: gather wait moved from before the last two MFMAs to just before the first consumer of a gathered row
# baseline (speedup 1.0000x reference)
.Lprio_e1_done:
	s_mov_b32 s93, s94
	s_add_u32 s94, s94, 0x1000
	s_cmp_lt_u32 s94, 0x61a8
	s_cselect_b32 s95, s94, s93
	s_lshl_b32 s95, s95, 9
	s_add_u32 s56, s8, s95
	s_addc_u32 s57, s9, 0
	ds_bpermute_b32 v126, v125, v51
	v_sub_f32_e32 v39, v48, v67
	v_fmamk_f32 v32, v39, 0x4297576a, v65
	v_fmamk_f32 v33, v39, 0x4297576a, v76
	v_med3_f32 v35, v32, s22, v74
	v_med3_f32 v37, v33, s22, v74
	v_mul_f32_e64 v32, v35, -v35
	v_fmamk_f32 v34, v35, 0x4019be61, v75
	v_mul_f32_e64 v33, v37, -v37
	v_fmamk_f32 v35, v35, 0xc019be61, v75
	v_exp_f32_e32 v32, v32
	v_exp_f32_e32 v33, v33
	v_exp_f32_e32 v36, v35
	v_fmamk_f32 v35, v37, 0x4019be61, v75
	v_exp_f32_e32 v34, v34
	v_exp_f32_e32 v35, v35
	v_fmamk_f32 v37, v37, 0xc019be61, v75
	v_exp_f32_e32 v37, v37
	v_pk_mul_f32 v[32:33], v[48:49], v[32:33] op_sel:[1,0]
	ds_read_b128 v[28:31], v69
	ds_read_b128 v[24:27], v69 offset:1024
	ds_read_b128 v[20:23], v69 offset:2048
	ds_read_b128 v[16:19], v69 offset:3072
	ds_read_b128 v[0:3], v70
	ds_read_b128 v[4:7], v70 offset:32
	ds_read_b128 v[8:11], v70 offset:64
	ds_read_b128 v[12:15], v70 offset:96
	v_pk_mul_f32 v[44:45], v[34:35], v[32:33]
	v_pk_mul_f32 v[34:35], v[34:35], s[16:17] op_sel_hi:[1,0]
	v_mov_b32_e32 v99, v80
	v_fmamk_f32 v38, v39, 0x4297576a, v77
	v_fmamk_f32 v39, v39, 0x4297576a, v78
	v_pk_mul_f32 v[46:47], v[34:35], v[44:45]
	v_pk_mul_f32 v[34:35], v[34:35], s[16:17] op_sel_hi:[1,0]
	v_pk_mul_f32 v[80:81], v[36:37], v[32:33]
	v_pk_mul_f32 v[36:37], v[36:37], s[16:17] op_sel_hi:[1,0]
	v_med3_f32 v41, v38, s22, v74
	v_med3_f32 v43, v39, s22, v74
	v_pk_mul_f32 v[58:59], v[34:35], v[46:47]
	v_pk_mul_f32 v[34:35], v[34:35], s[16:17] op_sel_hi:[1,0]
	v_pk_mul_f32 v[82:83], v[36:37], v[80:81]
	v_pk_mul_f32 v[36:37], v[36:37], s[16:17] op_sel_hi:[1,0]
	v_mul_f32_e64 v38, v41, -v41
	v_fmamk_f32 v40, v41, 0x4019be61, v75
	v_mul_f32_e64 v39, v43, -v43
	v_fmamk_f32 v41, v41, 0xc019be61, v75
	v_pk_mul_f32 v[34:35], v[34:35], v[58:59]
	v_pk_mul_f32 v[36:37], v[36:37], v[82:83]
	v_exp_f32_e32 v38, v38
	v_exp_f32_e32 v39, v39
	v_exp_f32_e32 v42, v41
	v_fmamk_f32 v41, v43, 0x4019be61, v75
	v_cvt_pk_f16_f32 v56, v44, v46
	v_cvt_pk_f16_f32 v54, v36, v82
	v_cvt_pk_f16_f32 v57, v58, v34
	v_cvt_pk_f16_f32 v55, v80, v32
	v_exp_f32_e32 v40, v40
	v_exp_f32_e32 v41, v41
	s_waitcnt lgkmcnt(0)
	v_mfma_f32_32x32x16_f16 v[0:15], v[28:31], v[54:57], v[0:15]
	v_mul_f32_e64 v38, v49, v38
	v_mul_f32_e64 v39, v49, v39
	v_fmamk_f32 v43, v43, 0xc019be61, v75
	v_mul_f32_e64 v84, v40, v38
	v_mul_f32_e64 v85, v41, v39
	v_pk_mul_f32 v[40:41], v[40:41], s[16:17] op_sel_hi:[1,0]
	v_cvt_pk_f16_f32 v30, v45, v47
	v_pk_mul_f32 v[86:87], v[40:41], v[84:85]
	v_pk_mul_f32 v[28:29], v[40:41], s[16:17] op_sel_hi:[1,0]
	v_cvt_pk_f16_f32 v31, v59, v35
	v_pk_mul_f32 v[40:41], v[28:29], v[86:87]
	v_pk_mul_f32 v[28:29], v[28:29], s[16:17] op_sel_hi:[1,0]
	v_exp_f32_e32 v43, v43
	v_pk_mul_f32 v[88:89], v[28:29], v[40:41]
	v_cvt_pk_f16_f32 v28, v37, v83
	v_cvt_pk_f16_f32 v29, v81, v33
	v_pk_mul_f32 v[36:37], v[42:43], v[38:39]
	v_pk_mul_f32 v[42:43], v[42:43], s[16:17] op_sel_hi:[1,0]
	v_mfma_f32_32x32x16_f16 v[0:15], v[24:27], v[28:31], v[0:15]
	v_mul_f32_e64 v32, v42, v36
	v_mul_f32_e64 v33, v43, v37
	v_mul_f32_e64 v24, v42, s16
	v_mul_f32_e64 v25, v43, s16
	v_cvt_pk_f16_f32 v26, v84, v86
	v_pk_mul_f32 v[34:35], v[24:25], v[32:33]
	v_cvt_pk_f16_f32 v27, v40, v88
	v_cvt_pk_f16_f32 v24, v34, v32
	v_cvt_pk_f16_f32 v25, v36, v38
	v_cvt_pk_f16_f32 v84, v85, v87
	v_cvt_pk_f16_f32 v82, v35, v33
	v_mfma_f32_32x32x16_f16 v[0:15], v[20:23], v[24:27], v[0:15]
	ds_read_b128 v[20:23], v69 offset:4096
	v_cvt_pk_f16_f32 v85, v41, v89
	v_cvt_pk_f16_f32 v83, v37, v39
	ds_read_b128 v[32:35], v70 offset:128
	ds_read_b128 v[36:39], v70 offset:160
	ds_read_b128 v[40:43], v70 offset:192
	ds_read_b128 v[44:47], v70 offset:224
	s_nop 0
	v_add_u32_e32 v64, s12, v64
	v_perm_b32 v127, v126, v51, s64
	s_nop 0
	v_readlane_b32 s70, v127, 0
	v_readlane_b32 s71, v127, 1
	v_readlane_b32 s72, v127, 2
	v_readlane_b32 s73, v127, 3
	v_readlane_b32 s74, v127, 4
	v_readlane_b32 s75, v127, 5
	v_readlane_b32 s76, v127, 6
	v_readlane_b32 s77, v127, 7
	v_readlane_b32 s78, v127, 8
	v_readlane_b32 s79, v127, 9
	v_readlane_b32 s80, v127, 10
	v_readlane_b32 s81, v127, 11
	v_readlane_b32 s82, v127, 12
	v_readlane_b32 s83, v127, 13
	v_readlane_b32 s84, v127, 14
	v_readlane_b32 s85, v127, 15
	s_pack_ll_b32_b16 s48, s70, 0
	v_mfma_f32_32x32x16_f16 v[0:15], v[16:19], v[82:85], v[0:15]
	ds_read_b128 v[16:19], v69 offset:5120
	s_nop 0
	s_lshl_b32 s48, s48, 8
	s_and_b32 s48, s48, 0xffff00
	s_pack_ll_b32_b16 s47, s71, 0
	s_add_u32 s48, s4, s48
	s_addc_u32 s49, s5, 0
	s_waitcnt lgkmcnt(1)
	v_mfma_f32_32x32x16_f16 v[32:47], v[20:23], v[54:57], v[32:47]
	ds_read_b128 v[20:23], v69 offset:6144
	s_lshl_b32 s47, s47, 8
	s_and_b32 s47, s47, 0xffff00
	s_pack_ll_b32_b16 s46, s72, 0
	s_pack_ll_b32_b16 s45, s73, 0
	s_pack_ll_b32_b16 s44, s74, 0
	s_pack_ll_b32_b16 s43, s75, 0
	s_waitcnt lgkmcnt(1)
	v_mfma_f32_32x32x16_f16 v[32:47], v[16:19], v[28:31], v[32:47]
	s_nop 0
	s_nop 0
	s_mov_b64 vcc, 0
	s_nop 0
	s_nop 0
	s_pack_ll_b32_b16 s3, s76, 0
	s_pack_ll_b32_b16 s2, s77, 0
	s_waitcnt lgkmcnt(0)
	v_mfma_f32_32x32x16_f16 v[32:47], v[20:23], v[24:27], v[32:47]
	s_nop 0
	s_nop 0
	s_pack_ll_b32_b16 s36, s78, 0
	s_pack_ll_b32_b16 s35, s79, 0
	s_pack_ll_b32_b16 s34, s80, 0
	s_pack_ll_b32_b16 s33, s81, 0
	s_pack_ll_b32_b16 s31, s82, 0
	s_pack_ll_b32_b16 s30, s83, 0
	s_pack_ll_b32_b16 s29, s84, 0
	s_pack_ll_b32_b16 s28, s85, 0
	s_pack_hh_b32_b16 s27, s70, 0
	s_pack_hh_b32_b16 s26, s71, 0
	s_pack_hh_b32_b16 s25, s72, 0
	s_pack_hh_b32_b16 s24, s73, 0
	s_pack_hh_b32_b16 s23, s74, 0
	s_pack_hh_b32_b16 s42, s75, 0
	s_pack_hh_b32_b16 s41, s76, 0
	s_pack_hh_b32_b16 s40, s77, 0
	s_pack_hh_b32_b16 s39, s78, 0
	s_pack_hh_b32_b16 s38, s79, 0
	s_pack_hh_b32_b16 s37, s80, 0
	s_pack_hh_b32_b16 s21, s81, 0
	s_pack_hh_b32_b16 s20, s82, 0
	s_pack_hh_b32_b16 s19, s83, 0
	s_pack_hh_b32_b16 s18, s84, 0
	s_pack_hh_b32_b16 s10, s85, 0
	ds_read_b128 v[16:19], v69 offset:7168
	s_nop 0
	global_load_dwordx4 v[56:59], v124, s[56:57]
	global_load_dword v80, v124, s[56:57] offset:24
	global_load_dword v51, v124, s[56:57] offset:-8
	global_load_dword v112, v79, s[48:49]
	s_add_u32 s48, s4, s47
	s_addc_u32 s49, s5, 0
	s_lshl_b32 s46, s46, 8
	s_and_b32 s46, s46, 0xffff00
	s_add_u32 s46, s4, s46
	s_addc_u32 s47, s5, 0
	s_lshl_b32 s45, s45, 8
	s_and_b32 s45, s45, 0xffff00
	global_load_dword v110, v79, s[48:49]
	global_load_dword v108, v79, s[46:47]
	s_add_u32 s46, s4, s45
	s_addc_u32 s47, s5, 0
	s_lshl_b32 s44, s44, 8
	s_and_b32 s44, s44, 0xffff00
	s_add_u32 s44, s4, s44
	s_addc_u32 s45, s5, 0
	s_lshl_b32 s43, s43, 8
	s_and_b32 s43, s43, 0xffff00
	global_load_dword v106, v79, s[46:47]
	global_load_dword v104, v79, s[44:45]
	s_add_u32 s44, s4, s43
	s_addc_u32 s45, s5, 0
	s_lshl_b32 s3, s3, 8
	s_and_b32 s3, s3, 0xffff00
	global_load_dword v102, v79, s[44:45]
	s_add_u32 s44, s4, s3
	s_addc_u32 s45, s5, 0
	s_lshl_b32 s2, s2, 8
	s_and_b32 s2, s2, 0xffff00
	s_add_u32 s2, s4, s2
	global_load_dword v100, v79, s[44:45]
	s_addc_u32 s3, s5, 0
	global_load_dword v114, v79, s[2:3]
	s_lshl_b32 s2, s36, 8
	s_and_b32 s2, s2, 0xffff00
	s_add_u32 s2, s4, s2
	s_addc_u32 s3, s5, 0
	global_load_dword v113, v79, s[2:3]
	s_lshl_b32 s2, s35, 8
	s_and_b32 s2, s2, 0xffff00
	s_add_u32 s2, s4, s2
	s_addc_u32 s3, s5, 0
	global_load_dword v111, v79, s[2:3]
	s_lshl_b32 s2, s34, 8
	s_and_b32 s2, s2, 0xffff00
	s_add_u32 s2, s4, s2
	s_addc_u32 s3, s5, 0
	global_load_dword v109, v79, s[2:3]
	s_lshl_b32 s2, s33, 8
	s_and_b32 s2, s2, 0xffff00
	s_add_u32 s2, s4, s2
	s_addc_u32 s3, s5, 0
	global_load_dword v107, v79, s[2:3]
	s_lshl_b32 s2, s31, 8
	s_and_b32 s2, s2, 0xffff00
	s_add_u32 s2, s4, s2
	s_addc_u32 s3, s5, 0
	global_load_dword v105, v79, s[2:3]
	s_lshl_b32 s2, s30, 8
	s_and_b32 s2, s2, 0xffff00
	s_add_u32 s2, s4, s2
	s_addc_u32 s3, s5, 0
	global_load_dword v103, v79, s[2:3]
	s_lshl_b32 s2, s29, 8
	s_and_b32 s2, s2, 0xffff00
	s_add_u32 s2, s4, s2
	s_addc_u32 s3, s5, 0
	global_load_dword v101, v79, s[2:3]
	s_lshl_b32 s2, s28, 8
	s_and_b32 s2, s2, 0xffff00
	s_add_u32 s2, s4, s2
	s_addc_u32 s3, s5, 0
	global_load_dword v98, v79, s[2:3]
	s_lshl_b32 s2, s27, 8
	s_and_b32 s2, s2, 0xffff00
	s_add_u32 s2, s4, s2
	s_addc_u32 s3, s5, 0
	global_load_dword v97, v79, s[2:3]
	s_lshl_b32 s2, s26, 8
	s_and_b32 s2, s2, 0xffff00
	s_add_u32 s2, s4, s2
	s_addc_u32 s3, s5, 0
	global_load_dword v96, v79, s[2:3]
	s_lshl_b32 s2, s25, 8
	s_and_b32 s2, s2, 0xffff00
	s_add_u32 s2, s4, s2
	s_addc_u32 s3, s5, 0
	global_load_dword v94, v79, s[2:3]
	s_lshl_b32 s2, s24, 8
	s_and_b32 s2, s2, 0xffff00
	s_add_u32 s2, s4, s2
	s_addc_u32 s3, s5, 0
	global_load_dword v91, v79, s[2:3]
	s_lshl_b32 s2, s23, 8
	s_and_b32 s2, s2, 0xffff00
	s_add_u32 s2, s4, s2
	s_addc_u32 s3, s5, 0
	global_load_dword v93, v79, s[2:3]
	s_lshl_b32 s2, s42, 8
	s_and_b32 s2, s2, 0xffff00
	s_add_u32 s2, s4, s2
	s_addc_u32 s3, s5, 0
	global_load_dword v90, v79, s[2:3]
	s_lshl_b32 s2, s41, 8
	s_and_b32 s2, s2, 0xffff00
	s_add_u32 s2, s4, s2
	s_addc_u32 s3, s5, 0
	global_load_dword v88, v79, s[2:3]
	s_lshl_b32 s2, s40, 8
	s_and_b32 s2, s2, 0xffff00
	s_add_u32 s2, s4, s2
	s_addc_u32 s3, s5, 0
	global_load_dword v86, v79, s[2:3]
	s_lshl_b32 s2, s39, 8
	s_and_b32 s2, s2, 0xffff00
	s_nop 0
	s_nop 0
	s_add_u32 s2, s4, s2
	s_waitcnt lgkmcnt(0)
	v_mfma_f32_32x32x16_f16 v[32:47], v[16:19], v[82:85], v[32:47]
	v_exp_f32_e32 v0, v0
	v_exp_f32_e32 v1, v1
	s_addc_u32 s3, s5, 0
	global_load_dword v85, v79, s[2:3]
	s_lshl_b32 s2, s38, 8
	s_and_b32 s2, s2, 0xffff00
	s_nop 0
	s_nop 0
	s_add_u32 s2, s4, s2
	v_exp_f32_e32 v6, v6
	v_exp_f32_e32 v7, v7
	s_addc_u32 s3, s5, 0
	global_load_dword v83, v79, s[2:3]
	s_lshl_b32 s2, s37, 8
	s_and_b32 s2, s2, 0xffff00
	s_add_u32 s2, s4, s2
	s_addc_u32 s3, s5, 0
	global_load_dword v92, v79, s[2:3]
	s_lshl_b32 s2, s21, 8
	s_and_b32 s2, s2, 0xffff00
	s_add_u32 s2, s4, s2
	s_addc_u32 s3, s5, 0
	global_load_dword v89, v79, s[2:3]
	s_lshl_b32 s2, s20, 8
	s_and_b32 s2, s2, 0xffff00
	s_add_u32 s2, s4, s2
	s_addc_u32 s3, s5, 0
	s_lshl_b32 s19, s19, 8
	s_and_b32 s19, s19, 0xffff00
	s_add_u32 s20, s4, s19
	s_addc_u32 s21, s5, 0
	s_lshl_b32 s18, s18, 8
	s_and_b32 s18, s18, 0xffff00
	s_add_u32 s18, s4, s18
	s_addc_u32 s19, s5, 0
	s_lshl_b32 s10, s10, 8
	s_and_b32 s10, s10, 0xffff00
	s_add_u32 s24, s4, s10
	s_addc_u32 s25, s5, 0
	global_load_dword v87, v79, s[2:3]
	global_load_dword v84, v79, s[20:21]
	global_load_dword v82, v79, s[18:19]
	global_load_dword v81, v79, s[24:25]
	v_pk_add_f32 v[0:1], v[0:1], 1.0 op_sel_hi:[1,0]
	s_nop 0
	s_nop 0
	v_exp_f32_e32 v16, v4
	v_exp_f32_e32 v17, v5
	v_log_f32_e32 v4, v0
	v_log_f32_e32 v5, v1
	s_nop 0
	s_nop 0
	v_exp_f32_e32 v2, v2
	v_exp_f32_e32 v3, v3
	v_pk_add_f32 v[6:7], v[6:7], 1.0 op_sel_hi:[1,0]
	v_log_f32_e32 v6, v6
	v_log_f32_e32 v7, v7
	v_pk_add_f32 v[0:1], v[16:17], 1.0 op_sel_hi:[1,0]
	v_pk_add_f32 v[2:3], v[2:3], 1.0 op_sel_hi:[1,0]
	v_log_f32_e32 v0, v0
	v_log_f32_e32 v1, v1
	v_exp_f32_e32 v18, v8
	v_exp_f32_e32 v19, v9
	v_log_f32_e32 v8, v2
	v_log_f32_e32 v9, v3
	v_pk_mul_f32 v[2:3], v[48:49], v[6:7] op_sel:[1,0]
	s_nop 0
	s_nop 0
	v_pk_mul_f32 v[0:1], v[48:49], v[0:1] op_sel:[1,0]
	s_nop 0
	s_nop 0
	v_cvt_pk_f16_f32 v3, v2, v3
	v_cvt_pk_f16_f32 v2, v0, v1
	v_pk_mul_f32 v[0:1], v[48:49], v[8:9] op_sel:[1,0]
	v_pk_mul_f32 v[4:5], v[48:49], v[4:5] op_sel:[1,0]
	s_nop 0
	s_nop 0
	s_nop 0
	s_nop 0
	v_cvt_pk_f16_f32 v1, v0, v1
	v_cvt_pk_f16_f32 v0, v4, v5
	v_pk_add_f32 v[4:5], v[18:19], 1.0 op_sel_hi:[1,0]
	v_exp_f32_e32 v6, v10
	v_exp_f32_e32 v7, v11
	v_exp_f32_e32 v8, v12
	v_exp_f32_e32 v9, v13
	v_exp_f32_e32 v10, v14
	v_exp_f32_e32 v11, v15
	v_pk_add_f32 v[8:9], v[8:9], 1.0 op_sel_hi:[1,0]
	v_pk_add_f32 v[10:11], v[10:11], 1.0 op_sel_hi:[1,0]
	v_pk_add_f32 v[6:7], v[6:7], 1.0 op_sel_hi:[1,0]
	v_log_f32_e32 v8, v8
	v_log_f32_e32 v9, v9
	v_log_f32_e32 v10, v10
	v_log_f32_e32 v11, v11
	ds_read_b128 v[12:15], v71
	v_log_f32_e32 v6, v6
	v_log_f32_e32 v7, v7
	v_log_f32_e32 v4, v4
	v_log_f32_e32 v5, v5
	v_pk_mul_f32 v[8:9], v[48:49], v[8:9] op_sel:[1,0]
	v_pk_mul_f32 v[10:11], v[48:49], v[10:11] op_sel:[1,0]
	v_cvt_pk_f16_f32 v118, v8, v9
	v_cvt_pk_f16_f32 v119, v10, v11
	v_pk_mul_f32 v[10:11], v[48:49], v[6:7] op_sel:[1,0]
	ds_read_b128 v[6:9], v71 offset:1024
	s_waitcnt lgkmcnt(1)
	v_mfma_f32_32x32x16_f16 v[16:31], v[0:3], v[12:15], 0
	s_nop 0
	s_nop 0
	v_mul_f32_e64 v4, v49, v4
	v_mul_f32_e64 v5, v49, v5
	v_exp_f32_e32 v32, v32
	v_exp_f32_e32 v33, v33
	s_nop 0
	s_nop 0
	v_cvt_pk_f16_f32 v117, v10, v11
	v_cvt_pk_f16_f32 v116, v4, v5
	v_exp_f32_e32 v36, v36
	v_exp_f32_e32 v37, v37
	v_pk_add_f32 v[32:33], v[32:33], 1.0 op_sel_hi:[1,0]
	s_waitcnt lgkmcnt(0)
	v_mfma_f32_32x32x16_f16 v[16:31], v[116:119], v[6:9], v[16:31]
	v_log_f32_e32 v54, v32
	v_log_f32_e32 v55, v33
	v_pk_add_f32 v[32:33], v[36:37], 1.0 op_sel_hi:[1,0]
	s_nop 0
	s_nop 0
	ds_read_b128 v[4:7], v71 offset:4096
	ds_read_b128 v[120:123], v71 offset:5120
	v_exp_f32_e32 v36, v38
	v_exp_f32_e32 v37, v39
	s_nop 0
	s_nop 0
	s_waitcnt lgkmcnt(1)
	v_mfma_f32_32x32x16_f16 v[0:15], v[0:3], v[4:7], 0
	v_exp_f32_e32 v34, v34
	v_exp_f32_e32 v35, v35
	v_pk_add_f32 v[36:37], v[36:37], 1.0 op_sel_hi:[1,0]
	v_log_f32_e32 v32, v32
	v_log_f32_e32 v33, v33
	v_log_f32_e32 v36, v36
	v_log_f32_e32 v37, v37
	v_pk_add_f32 v[34:35], v[34:35], 1.0 op_sel_hi:[1,0]
	v_pk_mul_f32 v[32:33], v[48:49], v[32:33] op_sel:[1,0]
	v_log_f32_e32 v38, v34
	v_log_f32_e32 v39, v35
	v_pk_mul_f32 v[34:35], v[48:49], v[36:37] op_sel:[1,0]
	v_pk_mul_f32 v[36:37], v[48:49], v[54:55] op_sel:[1,0]
	v_cvt_pk_f16_f32 v35, v34, v35
	v_cvt_pk_f16_f32 v34, v32, v33
	v_pk_mul_f32 v[32:33], v[48:49], v[38:39] op_sel:[1,0]
	s_waitcnt lgkmcnt(0)
	v_mfma_f32_32x32x16_f16 v[0:15], v[116:119], v[120:123], v[0:15]
	v_cvt_pk_f16_f32 v33, v32, v33
	v_cvt_pk_f16_f32 v32, v36, v37
	ds_read_b128 v[36:39], v71 offset:2048
	ds_read_b128 v[116:119], v71 offset:3072
	s_nop 0
	s_nop 0
	v_exp_f32_e32 v55, v44
	v_exp_f32_e32 v115, v45
	s_waitcnt lgkmcnt(1)
	v_mfma_f32_32x32x16_f16 v[16:31], v[32:35], v[36:39], v[16:31]
	ds_read_b128 v[36:39], v71 offset:6144
	v_exp_f32_e32 v44, v40
	v_exp_f32_e32 v45, v41
	v_exp_f32_e32 v52, v42
	v_exp_f32_e32 v54, v43
	ds_read_b128 v[40:43], v71 offset:7168
	s_nop 0
	s_waitcnt lgkmcnt(1)
	v_mfma_f32_32x32x16_f16 v[0:15], v[32:35], v[36:39], v[0:15]
	v_add_f32_e64 v34, v44, 1.0
	v_add_f32_e64 v35, v45, 1.0
	s_nop 0
	s_nop 0
	s_nop 0
	v_log_f32_e32 v36, v34
	v_log_f32_e32 v37, v35
	v_exp_f32_e32 v34, v46
	v_exp_f32_e32 v35, v47
	s_nop 0
	s_nop 0
	v_add_f32_e64 v32, v55, 1.0
	v_add_f32_e64 v33, v115, 1.0
	v_pk_add_f32 v[34:35], v[34:35], 1.0 op_sel_hi:[1,0]
	v_log_f32_e32 v32, v32
	v_log_f32_e32 v33, v33
	v_log_f32_e32 v34, v34
	v_log_f32_e32 v35, v35
	v_add_f32_e64 v38, v52, 1.0
	v_add_f32_e64 v39, v54, 1.0
	v_pk_mul_f32 v[32:33], v[48:49], v[32:33] op_sel:[1,0]
	v_log_f32_e32 v38, v38
	v_log_f32_e32 v39, v39
	v_pk_mul_f32 v[34:35], v[48:49], v[34:35] op_sel:[1,0]
	v_pk_mul_f32 v[36:37], v[48:49], v[36:37] op_sel:[1,0]
	v_cvt_pk_f16_f32 v35, v34, v35
	v_cvt_pk_f16_f32 v34, v32, v33
	v_pk_mul_f32 v[32:33], v[48:49], v[38:39] op_sel:[1,0]
	v_mov_b32_e32 v54, v53
	v_cvt_pk_f16_f32 v33, v32, v33
	v_cvt_pk_f16_f32 v32, v36, v37
	v_cvt_f16_f32_e32 v36, v49
	v_mov_b32_e32 v55, v53
	v_mfma_f32_32x32x16_f16 v[16:31], v[32:35], v[116:119], v[16:31]
	v_cmp_ne_u32_sdwa s[20:21], v95, v50 src0_sel:DWORD src1_sel:WORD_1
	v_cmp_ne_u32_sdwa s[18:19], v99, v50 src0_sel:WORD_1 src1_sel:WORD_1
	s_bitcmp1_b32 s20, 0
	v_cmp_lt_i32_e64 s[2:3], s13, v64
	s_cselect_b64 s[20:21], -1, 0
	s_bitcmp0_b32 s18, 0
	s_waitcnt lgkmcnt(0)
	v_mfma_f32_32x32x16_f16 v[0:15], v[32:35], v[40:43], v[0:15]
	v_cndmask_b32_e64 v32, 0, v36, s[0:1]
	v_pack_b32_f16 v52, v32, 0
	ds_read_b128 v[32:35], v72
	ds_read_b128 v[36:39], v72 offset:1024
	s_nop 0
	s_nop 0
	s_waitcnt lgkmcnt(1)
	v_mfma_f32_32x32x16_f16 v[16:31], v[52:55], v[32:35], v[16:31]
	v_mov_b64_e32 v[32:33], 0
	s_nop 0
	s_waitcnt lgkmcnt(0)
	v_mfma_f32_32x32x16_f16 v[0:15], v[52:55], v[36:39], v[0:15]
	s_nop 11
	v_permlane32_swap_b32_e32 v16, v0
	v_permlane32_swap_b32_e32 v17, v1
	v_permlane32_swap_b32_e32 v18, v2
	v_permlane32_swap_b32_e32 v19, v3
	v_permlane32_swap_b32_e32 v20, v4
	v_permlane32_swap_b32_e32 v21, v5
	v_permlane32_swap_b32_e32 v22, v6
	v_permlane32_swap_b32_e32 v23, v7
	v_permlane32_swap_b32_e32 v24, v8
	v_permlane32_swap_b32_e32 v25, v9
	v_permlane32_swap_b32_e32 v26, v10
	v_permlane32_swap_b32_e32 v27, v11
	v_permlane32_swap_b32_e32 v28, v12
	v_permlane32_swap_b32_e32 v29, v13
	v_permlane32_swap_b32_e32 v30, v14
	v_permlane32_swap_b32_e32 v31, v15
	s_waitcnt vmcnt(0)
	v_fma_mix_f32 v32, v16, v112, v32 op_sel:[0,1,0] op_sel_hi:[0,1,0]
	v_fma_mix_f32 v33, v16, v112, v33 op_sel_hi:[0,1,0]
	s_cbranch_scc1 .LBB4_13
	v_readlane_b32 s10, v50, 0
	s_bfe_u32 s19, s10, 0x80008
	v_lshl_or_b32 v16, s19, 7, v73
	ds_read_u16 v16, v16
	s_bfe_u32 s10, s10, 0x100010
	s_lshl_b32 s10, s10, 8
	s_add_u32 s58, s60, s10
	s_addc_u32 s59, s61, 0
	s_cmp_lg_u64 s[20:21], 0
	s_cselect_b32 s58, s58, s62
	s_cselect_b32 s59, s59, s63
	s_nop 0
	s_waitcnt lgkmcnt(0)
	v_fma_mix_f32 v16, v16, v33, v32 op_sel_hi:[1,0,0]
	s_nop 0
	s_mov_b64 s[20:21], -1
	v_mov_b64_e32 v[32:33], 0
	s_nop 0
	global_store_dword v79, v16, s[58:59] sc1
